# speedup vs baseline: 1.0196x; 1.0196x over previous
.LBB1_77:
	s_or_b64 exec, exec, s[42:43]
	v_sub_f32_e32 v115, v150, v174
	v_sub_f32_e32 v134, v150, v142
	v_add_f32_e64 v115, |v115|, |v134|
	v_sub_f32_e32 v134, v150, v144
	v_add_f32_e64 v115, v115, |v134|
	v_sub_f32_e32 v134, v151, v175
	v_sub_f32_e32 v135, v151, v143
	v_add_f32_e64 v134, |v134|, |v135|
	v_sub_f32_e32 v135, v151, v145
	v_fma_f32 v115, v116, v115, 0
	v_add_f32_e32 v116, 0, v116
	v_add_f32_e64 v134, v134, |v135|
	v_fmac_f32_e32 v115, v117, v134
	v_add_f32_e32 v116, v117, v116
	v_sub_f32_e32 v117, v152, v172
	v_sub_f32_e32 v134, v152, v138
	v_add_f32_e64 v117, |v117|, |v134|
	v_sub_f32_e32 v134, v152, v140
	v_add_f32_e64 v117, v117, |v134|
	v_fmac_f32_e32 v115, v166, v117
	v_sub_f32_e32 v117, v153, v173
	v_sub_f32_e32 v134, v153, v139
	v_add_f32_e64 v117, |v117|, |v134|
	v_sub_f32_e32 v134, v153, v141
	v_add_f32_e64 v117, v117, |v134|
	v_fmac_f32_e32 v115, v167, v117
	v_add_f32_e32 v116, v166, v116
	v_add_f32_e32 v116, v167, v116
	v_mov_b32_e32 v246, v115
	v_mov_b32_e32 v247, v116
.LBB1_80:
	s_or_b64 exec, exec, s[24:25]
	v_mad_u32_u24 v115, v233, s53, v226
	s_waitcnt lgkmcnt(0)
	s_barrier
	ds_read_b128 v[134:137], v115
	ds_read_b128 v[138:141], v115 offset:64
	s_waitcnt lgkmcnt(1)
	v_mfma_f32_16x16x32_bf16 v[116:119], v[46:49], v[134:137], v[118:121]
	v_add_u32_e32 v166, v191, v229
	v_mov_b32_e32 v167, v114
	s_mov_b32 s46, 0
	v_mfma_f32_16x16x32_bf16 v[120:123], v[74:77], v[134:137], v[122:125]
	v_mfma_f32_16x16x32_bf16 v[126:129], v[18:21], v[134:137], v[126:129]
	s_waitcnt lgkmcnt(0)
	v_mfma_f32_16x16x32_bf16 v[116:119], v[50:53], v[138:141], v[116:119]
	v_mfma_f32_16x16x32_bf16 v[120:123], v[78:81], v[138:141], v[120:123]
	v_mfma_f32_16x16x32_bf16 v[126:129], v[22:25], v[138:141], v[126:129]
	s_and_b64 s[70:71], exec, s[6:7]
	s_cbranch_scc1 .Lred_skip_0
	v_add_f32_dpp v246, v246, v246 quad_perm:[1,0,3,2] row_mask:0xf bank_mask:0xf bound_ctrl:1
	v_add_f32_dpp v247, v247, v247 quad_perm:[1,0,3,2] row_mask:0xf bank_mask:0xf bound_ctrl:1
	s_nop 0
	v_add_f32_dpp v246, v246, v246 quad_perm:[2,3,0,1] row_mask:0xf bank_mask:0xf bound_ctrl:1
	v_add_f32_dpp v247, v247, v247 quad_perm:[2,3,0,1] row_mask:0xf bank_mask:0xf bound_ctrl:1
	s_nop 0
	v_add_f32_dpp v246, v246, v246 row_half_mirror row_mask:0xf bank_mask:0xf bound_ctrl:1
	v_add_f32_dpp v247, v247, v247 row_half_mirror row_mask:0xf bank_mask:0xf bound_ctrl:1
	s_nop 0
	v_add_f32_dpp v246, v246, v246 row_mirror row_mask:0xf bank_mask:0xf bound_ctrl:1
	v_add_f32_dpp v247, v247, v247 row_mirror row_mask:0xf bank_mask:0xf bound_ctrl:1
	s_nop 0
	v_readlane_b32 s62, v246, 0
	v_readlane_b32 s63, v247, 0
	v_readlane_b32 s64, v246, 16
	v_readlane_b32 s65, v247, 16
	v_readlane_b32 s66, v246, 32
	v_readlane_b32 s67, v247, 32
	v_readlane_b32 s68, v246, 48
	v_readlane_b32 s69, v247, 48
	v_mov_b32_e32 v246, s64
	v_mov_b32_e32 v247, s65
	s_nop 0
	v_pk_add_f32 v[246:247], s[62:63], v[246:247]
	s_nop 0
	v_pk_add_f32 v[246:247], v[246:247], s[66:67]
	s_nop 0
	v_pk_add_f32 v[246:247], v[246:247], s[68:69]
	s_and_saveexec_b64 s[70:71], s[18:19]
	ds_write_b64 v231, v[246:247]
	s_or_b64 exec, exec, s[70:71]
.Lred_skip_0:
	s_nop 5
	v_exp_f32_e32 v115, v116
	v_med3_f32 v116, v120, s55, v232
	v_exp_f32_e32 v125, v116
	v_mfma_f32_16x16x32_bf16 v[130:133], v[102:105], v[134:137], v[130:133]
	v_med3_f32 v121, v121, s55, v232
	v_exp_f32_e32 v124, v126
	v_exp_f32_e32 v126, v127
	v_exp_f32_e32 v127, v121
	v_mfma_f32_16x16x32_bf16 v[130:133], v[106:109], v[138:141], v[130:133]
	v_exp_f32_e32 v117, v117
	v_add_f32_e32 v115, 1.0, v115
	v_pk_add_f32 v[134:135], v[124:125], 1.0 op_sel_hi:[1,0]
	v_rcp_f32_e32 v120, v115
	v_mul_f32_e32 v115, v134, v135
	v_pk_add_f32 v[134:135], v[126:127], 1.0 op_sel_hi:[1,0]
	s_nop 1
	v_exp_f32_e32 v116, v130
	v_rcp_f32_e32 v130, v115
	v_add_f32_e32 v115, 1.0, v117
	v_mul_f32_e32 v117, v134, v135
	v_exp_f32_e32 v124, v131
	v_rcp_f32_e32 v131, v117
	v_rcp_f32_e32 v121, v115
	v_mov_b32_e32 v126, v125
	v_pk_add_f32 v[126:127], v[126:127], 1.0 op_sel_hi:[1,0] neg_lo:[1,0] neg_hi:[1,0]
	v_med3_f32 v123, v123, s55, v232
	v_pk_mul_f32 v[126:127], v[126:127], v[130:131]
	v_exp_f32_e32 v119, v119
	v_pk_fma_f32 v[168:169], v[168:169], v[120:121], v[126:127]
	s_nop 0
	v_mul_f32_e32 v115, 0xc038aa3b, v168
	v_med3_f32 v115, v115, s55, v232
	v_exp_f32_e32 v117, v115
	v_mul_f32_e32 v115, 0xc038aa3b, v169
	v_med3_f32 v115, v115, s55, v232
	v_exp_f32_e32 v125, v115
	v_pk_add_f32 v[120:121], v[116:117], 1.0 op_sel_hi:[1,0]
	v_pk_add_f32 v[126:127], v[124:125], 1.0 op_sel_hi:[1,0]
	v_mul_f32_e32 v115, v120, v121
	v_rcp_f32_e32 v120, v115
	v_mul_f32_e32 v115, v126, v127
	v_rcp_f32_e32 v121, v115
	v_mov_b32_e32 v124, v117
	v_exp_f32_e32 v115, v118
	v_med3_f32 v118, v122, s55, v232
	v_pk_add_f32 v[116:117], v[124:125], 1.0 op_sel_hi:[1,0] neg_lo:[1,0] neg_hi:[1,0]
	v_exp_f32_e32 v124, v128
	v_exp_f32_e32 v125, v118
	v_add_f32_e32 v115, 1.0, v115
	v_rcp_f32_e32 v122, v115
	v_exp_f32_e32 v118, v132
	v_pk_add_f32 v[126:127], v[124:125], 1.0 op_sel_hi:[1,0]
	v_exp_f32_e32 v124, v133
	v_mul_f32_e32 v115, v126, v127
	v_exp_f32_e32 v126, v129
	v_exp_f32_e32 v127, v123
	v_rcp_f32_e32 v128, v115
	v_add_f32_e32 v115, 1.0, v119
	v_rcp_f32_e32 v123, v115
	v_pk_add_f32 v[130:131], v[126:127], 1.0 op_sel_hi:[1,0]
	v_mov_b32_e32 v126, v125
	v_mul_f32_e32 v119, v130, v131
	v_rcp_f32_e32 v129, v119
	v_pk_add_f32 v[126:127], v[126:127], 1.0 op_sel_hi:[1,0] neg_lo:[1,0] neg_hi:[1,0]
	v_pk_mul_f32 v[116:117], v[116:117], v[120:121]
	v_pk_mul_f32 v[126:127], v[126:127], v[128:129]
	s_nop 0
	v_pk_fma_f32 v[170:171], v[170:171], v[122:123], v[126:127]
	v_cvt_pk_bf16_f32 v120, v116, v117
	v_mul_f32_e32 v115, 0xc038aa3b, v170
	v_med3_f32 v115, v115, s55, v232
	v_exp_f32_e32 v119, v115
	v_mul_f32_e32 v115, 0xc038aa3b, v171
	v_med3_f32 v115, v115, s55, v232
	v_exp_f32_e32 v125, v115
	v_pk_add_f32 v[122:123], v[118:119], 1.0 op_sel_hi:[1,0]
	v_pk_mul_f32 v[116:117], v[162:163], v[116:117]
	v_mul_f32_e32 v115, v122, v123
	v_pk_add_f32 v[126:127], v[124:125], 1.0 op_sel_hi:[1,0]
	v_rcp_f32_e32 v122, v115
	v_mul_f32_e32 v115, v126, v127
	v_rcp_f32_e32 v123, v115
	v_mov_b32_e32 v124, v119
	v_pk_add_f32 v[118:119], v[124:125], 1.0 op_sel_hi:[1,0] neg_lo:[1,0] neg_hi:[1,0]
	v_cvt_pk_bf16_f32 v116, v116, v117
	v_pk_mul_f32 v[118:119], v[118:119], v[122:123]
	v_lshl_add_u64 v[122:123], v[166:167], 1, s[30:31]
	v_cvt_pk_bf16_f32 v121, v118, v119
	v_pk_mul_f32 v[118:119], v[164:165], v[118:119]
	global_store_dwordx2 v[122:123], v[120:121], off nt
	v_cvt_pk_bf16_f32 v117, v118, v119
	ds_write_b64 v205, v[116:117] offset:4608
	s_waitcnt lgkmcnt(0)
	s_barrier
	ds_read_b128 v[146:149], v206 offset:4608
	ds_read_b128 v[142:145], v206 offset:4672
	ds_read_b128 v[138:141], v206 offset:4736
	ds_read_b128 v[134:137], v206 offset:4800
	v_or_b32_e32 v167, 16, v233
	s_and_saveexec_b64 s[24:25], s[6:7]
	s_xor_b64 s[24:25], exec, s[24:25]
	s_cbranch_execz .LBB1_91
	s_and_saveexec_b64 s[42:43], s[8:9]
	s_xor_b64 s[42:43], exec, s[42:43]
	s_cbranch_execz .LBB1_88
	s_cmpk_eq_i32 s40, 0x1810
	s_cbranch_scc1 .LBB1_88
	s_waitcnt vmcnt(4)
	v_fma_f32 v115, v188, v178, v179
	v_max_f32_e32 v115, 0, v115
	v_mul_f32_e32 v115, 0xbfb8aa3b, v115
	v_exp_f32_e32 v115, v115
	s_bitcmp1_b32 s59, 0
	s_waitcnt vmcnt(3)
	v_fma_f32 v116, v178, v187, v179
	s_cselect_b32 s47, 0, 0x1200
	v_cvt_pk_bf16_f32 v115, v115, s0
	ds_write_b16 v213, v115
	v_max_f32_e32 v115, 0, v116
	v_cvt_pk_bf16_f32 v116, v188, s0
	v_lshl_add_u32 v117, s47, 1, v221
	v_mul_f32_e32 v115, 0xbfb8aa3b, v115
	ds_write_b16 v117, v116
	s_waitcnt vmcnt(2)
	v_fma_f32 v116, v178, v186, v179
	v_exp_f32_e32 v115, v115
	v_max_f32_e32 v116, 0, v116
	v_mul_f32_e32 v116, 0xbfb8aa3b, v116
	v_exp_f32_e32 v116, v116
	v_cvt_pk_bf16_f32 v115, v115, s0
	ds_write_b16 v213, v115 offset:3584
	v_cvt_pk_bf16_f32 v115, v187, s0
	ds_write_b16 v117, v115 offset:2304
	v_cvt_pk_bf16_f32 v115, v116, s0
	s_waitcnt vmcnt(1)
	v_fma_f32 v116, v178, v157, v179
	v_max_f32_e32 v116, 0, v116
	v_mul_f32_e32 v116, 0xbfb8aa3b, v116
	v_exp_f32_e32 v116, v116
	ds_write_b16 v213, v115 offset:7168
	v_cvt_pk_bf16_f32 v115, v186, s0
	ds_write_b16 v117, v115 offset:4608
	v_cvt_pk_bf16_f32 v115, v116, s0
	ds_write_b16 v213, v115 offset:10752
	v_cvt_pk_bf16_f32 v115, v157, s0
	ds_write_b16 v117, v115 offset:6912
	s_and_saveexec_b64 s[44:45], s[26:27]
	s_cbranch_execz .LBB1_85
	v_fma_f32 v115, v155, v180, v181
	v_max_f32_e32 v115, 0, v115
	v_mul_f32_e32 v115, 0xbfb8aa3b, v115
	v_exp_f32_e32 v115, v115
	v_fma_f32 v116, v180, v182, v181
	v_max_f32_e32 v116, 0, v116
	v_mul_f32_e32 v116, 0xbfb8aa3b, v116
	v_cvt_pk_bf16_f32 v115, v115, s0
	ds_write_b16 v214, v115
	v_exp_f32_e32 v115, v116
	v_cvt_pk_bf16_f32 v116, v155, s0
	v_lshl_add_u32 v117, s47, 1, v222
	ds_write_b16 v117, v116
	v_fma_f32 v116, v180, v183, v181
	v_max_f32_e32 v116, 0, v116
	v_mul_f32_e32 v116, 0xbfb8aa3b, v116
	v_exp_f32_e32 v116, v116
	v_cvt_pk_bf16_f32 v115, v115, s0
	ds_write_b16 v214, v115 offset:3584
	v_cvt_pk_bf16_f32 v115, v182, s0
	ds_write_b16 v117, v115 offset:2304
	v_cvt_pk_bf16_f32 v115, v116, s0
	v_fma_f32 v116, v180, v184, v181
	v_max_f32_e32 v116, 0, v116
	v_mul_f32_e32 v116, 0xbfb8aa3b, v116
	v_exp_f32_e32 v116, v116
	ds_write_b16 v214, v115 offset:7168
	v_cvt_pk_bf16_f32 v115, v183, s0
	ds_write_b16 v117, v115 offset:4608
	v_cvt_pk_bf16_f32 v115, v116, s0
	ds_write_b16 v214, v115 offset:10752
	v_cvt_pk_bf16_f32 v115, v184, s0
	ds_write_b16 v117, v115 offset:6912

.LBB1_113:
	s_or_b64 exec, exec, s[42:43]
	v_sub_f32_e32 v115, v150, v176
	v_sub_f32_e32 v134, v150, v142
	v_add_f32_e64 v115, |v115|, |v134|
	v_sub_f32_e32 v134, v150, v144
	v_add_f32_e64 v115, v115, |v134|
	v_sub_f32_e32 v134, v151, v177
	v_sub_f32_e32 v135, v151, v143
	v_add_f32_e64 v134, |v134|, |v135|
	v_sub_f32_e32 v135, v151, v145
	v_fma_f32 v115, v116, v115, 0
	v_add_f32_e32 v116, 0, v116
	v_add_f32_e64 v134, v134, |v135|
	v_fmac_f32_e32 v115, v117, v134
	v_add_f32_e32 v116, v117, v116
	v_sub_f32_e32 v117, v152, v174
	v_sub_f32_e32 v134, v152, v138
	v_add_f32_e64 v117, |v117|, |v134|
	v_sub_f32_e32 v134, v152, v140
	v_add_f32_e64 v117, v117, |v134|
	v_fmac_f32_e32 v115, v172, v117
	v_sub_f32_e32 v117, v153, v175
	v_sub_f32_e32 v134, v153, v139
	v_add_f32_e64 v117, |v117|, |v134|
	v_sub_f32_e32 v134, v153, v141
	v_add_f32_e64 v117, v117, |v134|
	v_fmac_f32_e32 v115, v173, v117
	v_add_f32_e32 v116, v172, v116
	v_add_f32_e32 v116, v173, v116
	v_mov_b32_e32 v246, v115
	v_mov_b32_e32 v247, v116
.LBB1_116:
	s_or_b64 exec, exec, s[24:25]
	v_mad_u32_u24 v115, v167, s53, v226
	s_waitcnt lgkmcnt(0)
	s_barrier
	ds_read_b128 v[134:137], v115
	ds_read_b128 v[138:141], v115 offset:64
	s_waitcnt lgkmcnt(1)
	v_mfma_f32_16x16x32_bf16 v[116:119], v[46:49], v[134:137], v[118:121]
	s_mov_b32 s46, 0
	v_or_b32_e32 v236, 32, v233
	v_mfma_f32_16x16x32_bf16 v[120:123], v[74:77], v[134:137], v[122:125]
	v_mfma_f32_16x16x32_bf16 v[126:129], v[18:21], v[134:137], v[126:129]
	s_waitcnt lgkmcnt(0)
	v_mfma_f32_16x16x32_bf16 v[116:119], v[50:53], v[138:141], v[116:119]
	v_mfma_f32_16x16x32_bf16 v[120:123], v[78:81], v[138:141], v[120:123]
	v_mfma_f32_16x16x32_bf16 v[126:129], v[22:25], v[138:141], v[126:129]
	s_and_b64 s[70:71], exec, s[6:7]
	s_cbranch_scc1 .Lred_skip_1
	v_add_f32_dpp v246, v246, v246 quad_perm:[1,0,3,2] row_mask:0xf bank_mask:0xf bound_ctrl:1
	v_add_f32_dpp v247, v247, v247 quad_perm:[1,0,3,2] row_mask:0xf bank_mask:0xf bound_ctrl:1
	s_nop 0
	v_add_f32_dpp v246, v246, v246 quad_perm:[2,3,0,1] row_mask:0xf bank_mask:0xf bound_ctrl:1
	v_add_f32_dpp v247, v247, v247 quad_perm:[2,3,0,1] row_mask:0xf bank_mask:0xf bound_ctrl:1
	s_nop 0
	v_add_f32_dpp v246, v246, v246 row_half_mirror row_mask:0xf bank_mask:0xf bound_ctrl:1
	v_add_f32_dpp v247, v247, v247 row_half_mirror row_mask:0xf bank_mask:0xf bound_ctrl:1
	s_nop 0
	v_add_f32_dpp v246, v246, v246 row_mirror row_mask:0xf bank_mask:0xf bound_ctrl:1
	v_add_f32_dpp v247, v247, v247 row_mirror row_mask:0xf bank_mask:0xf bound_ctrl:1
	s_nop 0
	v_readlane_b32 s62, v246, 0
	v_readlane_b32 s63, v247, 0
	v_readlane_b32 s64, v246, 16
	v_readlane_b32 s65, v247, 16
	v_readlane_b32 s66, v246, 32
	v_readlane_b32 s67, v247, 32
	v_readlane_b32 s68, v246, 48
	v_readlane_b32 s69, v247, 48
	v_mov_b32_e32 v246, s64
	v_mov_b32_e32 v247, s65
	s_nop 0
	v_pk_add_f32 v[246:247], s[62:63], v[246:247]
	s_nop 0
	v_pk_add_f32 v[246:247], v[246:247], s[66:67]
	s_nop 0
	v_pk_add_f32 v[246:247], v[246:247], s[68:69]
	s_and_saveexec_b64 s[70:71], s[18:19]
	ds_write_b64 v231, v[246:247] offset:24
	s_or_b64 exec, exec, s[70:71]
.Lred_skip_1:
	s_nop 5
	v_exp_f32_e32 v115, v116
	v_med3_f32 v116, v120, s55, v232
	v_exp_f32_e32 v125, v116
	v_mfma_f32_16x16x32_bf16 v[130:133], v[102:105], v[134:137], v[130:133]
	v_med3_f32 v121, v121, s55, v232
	v_exp_f32_e32 v124, v126
	v_exp_f32_e32 v126, v127
	v_exp_f32_e32 v127, v121
	v_mfma_f32_16x16x32_bf16 v[130:133], v[106:109], v[138:141], v[130:133]
	v_exp_f32_e32 v117, v117
	v_add_f32_e32 v115, 1.0, v115
	v_pk_add_f32 v[134:135], v[124:125], 1.0 op_sel_hi:[1,0]
	v_rcp_f32_e32 v120, v115
	v_mul_f32_e32 v115, v134, v135
	v_pk_add_f32 v[134:135], v[126:127], 1.0 op_sel_hi:[1,0]
	s_nop 1
	v_exp_f32_e32 v116, v130
	v_rcp_f32_e32 v130, v115
	v_add_f32_e32 v115, 1.0, v117
	v_mul_f32_e32 v117, v134, v135
	v_exp_f32_e32 v124, v131
	v_rcp_f32_e32 v131, v117
	v_rcp_f32_e32 v121, v115
	v_mov_b32_e32 v126, v125
	v_pk_add_f32 v[126:127], v[126:127], 1.0 op_sel_hi:[1,0] neg_lo:[1,0] neg_hi:[1,0]
	v_med3_f32 v123, v123, s55, v232
	v_pk_mul_f32 v[126:127], v[126:127], v[130:131]
	v_exp_f32_e32 v119, v119
	v_pk_fma_f32 v[168:169], v[168:169], v[120:121], v[126:127]
	s_nop 0
	v_mul_f32_e32 v115, 0xc038aa3b, v168
	v_med3_f32 v115, v115, s55, v232
	v_exp_f32_e32 v117, v115
	v_mul_f32_e32 v115, 0xc038aa3b, v169
	v_med3_f32 v115, v115, s55, v232
	v_exp_f32_e32 v125, v115
	v_pk_add_f32 v[120:121], v[116:117], 1.0 op_sel_hi:[1,0]
	v_pk_add_f32 v[126:127], v[124:125], 1.0 op_sel_hi:[1,0]
	v_mul_f32_e32 v115, v120, v121
	v_rcp_f32_e32 v120, v115
	v_mul_f32_e32 v115, v126, v127
	v_rcp_f32_e32 v121, v115
	v_mov_b32_e32 v124, v117
	v_exp_f32_e32 v115, v118
	v_med3_f32 v118, v122, s55, v232
	v_pk_add_f32 v[116:117], v[124:125], 1.0 op_sel_hi:[1,0] neg_lo:[1,0] neg_hi:[1,0]
	v_exp_f32_e32 v124, v128
	v_exp_f32_e32 v125, v118
	v_add_f32_e32 v115, 1.0, v115
	v_rcp_f32_e32 v122, v115
	v_exp_f32_e32 v118, v132
	v_pk_add_f32 v[126:127], v[124:125], 1.0 op_sel_hi:[1,0]
	v_exp_f32_e32 v124, v133
	v_mul_f32_e32 v115, v126, v127
	v_exp_f32_e32 v126, v129
	v_exp_f32_e32 v127, v123
	v_rcp_f32_e32 v128, v115
	v_add_f32_e32 v115, 1.0, v119
	v_rcp_f32_e32 v123, v115
	v_pk_add_f32 v[130:131], v[126:127], 1.0 op_sel_hi:[1,0]
	v_mov_b32_e32 v126, v125
	v_mul_f32_e32 v119, v130, v131
	v_rcp_f32_e32 v129, v119
	v_pk_add_f32 v[126:127], v[126:127], 1.0 op_sel_hi:[1,0] neg_lo:[1,0] neg_hi:[1,0]
	v_pk_mul_f32 v[116:117], v[116:117], v[120:121]
	v_pk_mul_f32 v[126:127], v[126:127], v[128:129]
	s_nop 0
	v_pk_fma_f32 v[170:171], v[170:171], v[122:123], v[126:127]
	v_cvt_pk_bf16_f32 v120, v116, v117
	v_mul_f32_e32 v115, 0xc038aa3b, v170
	v_med3_f32 v115, v115, s55, v232
	v_exp_f32_e32 v119, v115
	v_mul_f32_e32 v115, 0xc038aa3b, v171
	v_med3_f32 v115, v115, s55, v232
	v_exp_f32_e32 v125, v115
	v_pk_add_f32 v[122:123], v[118:119], 1.0 op_sel_hi:[1,0]
	v_pk_mul_f32 v[116:117], v[162:163], v[116:117]
	v_mul_f32_e32 v115, v122, v123
	v_pk_add_f32 v[126:127], v[124:125], 1.0 op_sel_hi:[1,0]
	v_rcp_f32_e32 v122, v115
	v_mul_f32_e32 v115, v126, v127
	v_rcp_f32_e32 v123, v115
	v_mov_b32_e32 v124, v119
	v_pk_add_f32 v[118:119], v[124:125], 1.0 op_sel_hi:[1,0] neg_lo:[1,0] neg_hi:[1,0]
	v_cvt_pk_bf16_f32 v116, v116, v117
	v_pk_mul_f32 v[118:119], v[118:119], v[122:123]
	v_add_u32_e32 v122, 0x80, v166
	v_cvt_pk_bf16_f32 v121, v118, v119
	v_mov_b32_e32 v123, v114
	v_pk_mul_f32 v[118:119], v[164:165], v[118:119]
	v_lshl_add_u64 v[122:123], v[122:123], 1, s[30:31]
	v_cvt_pk_bf16_f32 v117, v118, v119
	global_store_dwordx2 v[122:123], v[120:121], off nt
	ds_write_b64 v205, v[116:117]
	s_waitcnt lgkmcnt(0)
	s_barrier
	ds_read_b128 v[146:149], v193
	ds_read_b128 v[142:145], v193 offset:64
	ds_read_b128 v[138:141], v193 offset:128
	ds_read_b128 v[134:137], v193 offset:192
	s_and_saveexec_b64 s[24:25], s[6:7]
	s_xor_b64 s[24:25], exec, s[24:25]
	s_cbranch_execz .LBB1_127
	s_and_saveexec_b64 s[42:43], s[8:9]
	s_xor_b64 s[42:43], exec, s[42:43]
	s_cbranch_execz .LBB1_124
	s_cmpk_eq_i32 s40, 0x1810
	s_cbranch_scc1 .LBB1_124
	s_bitcmp1_b32 s59, 0
	s_cselect_b32 s47, 0, 0x1c00
	s_waitcnt vmcnt(4)
	v_cvt_pk_bf16_f32 v115, v188, s0
	v_lshl_add_u32 v116, s47, 1, v223
	ds_write_b16 v116, v115 offset:80
	ds_write_b16 v213, v115 offset:80
	s_waitcnt vmcnt(3)
	v_cvt_pk_bf16_f32 v115, v187, s0
	ds_write_b16 v116, v115 offset:3664
	ds_write_b16 v215, v115 offset:80
	s_waitcnt vmcnt(2)
	v_cvt_pk_bf16_f32 v115, v186, s0
	ds_write_b16 v116, v115 offset:7248
	ds_write_b16 v216, v115 offset:80
	s_waitcnt vmcnt(1)
	v_cvt_pk_bf16_f32 v115, v157, s0
	ds_write_b16 v116, v115 offset:10832
	ds_write_b16 v217, v115 offset:80
	s_and_saveexec_b64 s[44:45], s[26:27]
	s_cbranch_execz .LBB1_121
	v_cvt_pk_bf16_f32 v115, v155, s0
	v_lshl_add_u32 v116, s47, 1, v224
	ds_write_b16 v116, v115 offset:80
	ds_write_b16 v214, v115 offset:80
	v_cvt_pk_bf16_f32 v115, v182, s0
	ds_write_b16 v116, v115 offset:3664
	ds_write_b16 v218, v115 offset:80
	v_cvt_pk_bf16_f32 v115, v183, s0
	ds_write_b16 v116, v115 offset:7248
	ds_write_b16 v219, v115 offset:80
	v_cvt_pk_bf16_f32 v115, v184, s0
	ds_write_b16 v116, v115 offset:10832
	ds_write_b16 v220, v115 offset:80

.LBB1_152:
	s_or_b64 exec, exec, s[24:25]
	v_mad_u32_u24 v115, v236, s53, v226
	s_waitcnt lgkmcnt(0)
	s_barrier
	ds_read_b128 v[134:137], v115
	ds_read_b128 v[138:141], v115 offset:64
	s_waitcnt lgkmcnt(1)
	v_mfma_f32_16x16x32_bf16 v[116:119], v[46:49], v[134:137], v[118:121]
	s_mov_b32 s48, 0
	s_cmpk_lg_i32 s40, 0x1810
	v_or_b32_e32 v167, 48, v233
	v_mfma_f32_16x16x32_bf16 v[120:123], v[74:77], v[134:137], v[122:125]
	s_cselect_b64 s[24:25], -1, 0
	v_mfma_f32_16x16x32_bf16 v[126:129], v[18:21], v[134:137], v[126:129]
	s_waitcnt lgkmcnt(0)
	v_mfma_f32_16x16x32_bf16 v[116:119], v[50:53], v[138:141], v[116:119]
	v_mfma_f32_16x16x32_bf16 v[120:123], v[78:81], v[138:141], v[120:123]
	v_mfma_f32_16x16x32_bf16 v[126:129], v[22:25], v[138:141], v[126:129]
	s_and_b64 s[70:71], exec, s[6:7]
	s_cbranch_scc1 .Lred_skip_2
	v_add_f32_dpp v246, v246, v246 quad_perm:[1,0,3,2] row_mask:0xf bank_mask:0xf bound_ctrl:1
	v_add_f32_dpp v247, v247, v247 quad_perm:[1,0,3,2] row_mask:0xf bank_mask:0xf bound_ctrl:1
	s_nop 0
	v_add_f32_dpp v246, v246, v246 quad_perm:[2,3,0,1] row_mask:0xf bank_mask:0xf bound_ctrl:1
	v_add_f32_dpp v247, v247, v247 quad_perm:[2,3,0,1] row_mask:0xf bank_mask:0xf bound_ctrl:1
	s_nop 0
	v_add_f32_dpp v246, v246, v246 row_half_mirror row_mask:0xf bank_mask:0xf bound_ctrl:1
	v_add_f32_dpp v247, v247, v247 row_half_mirror row_mask:0xf bank_mask:0xf bound_ctrl:1
	s_nop 0
	v_add_f32_dpp v246, v246, v246 row_mirror row_mask:0xf bank_mask:0xf bound_ctrl:1
	v_add_f32_dpp v247, v247, v247 row_mirror row_mask:0xf bank_mask:0xf bound_ctrl:1
	s_nop 0
	v_readlane_b32 s62, v246, 0
	v_readlane_b32 s63, v247, 0
	v_readlane_b32 s64, v246, 16
	v_readlane_b32 s65, v247, 16
	v_readlane_b32 s66, v246, 32
	v_readlane_b32 s67, v247, 32
	v_readlane_b32 s68, v246, 48
	v_readlane_b32 s69, v247, 48
	v_mov_b32_e32 v246, s64
	v_mov_b32_e32 v247, s65
	s_nop 0
	v_pk_add_f32 v[246:247], s[62:63], v[246:247]
	s_nop 0
	v_pk_add_f32 v[246:247], v[246:247], s[66:67]
	s_nop 0
	v_pk_add_f32 v[246:247], v[246:247], s[68:69]
	s_and_saveexec_b64 s[70:71], s[18:19]
	ds_write_b64 v231, v[246:247] offset:48
	s_or_b64 exec, exec, s[70:71]
.Lred_skip_2:
	s_nop 5
	v_exp_f32_e32 v115, v116
	v_med3_f32 v116, v120, s55, v232
	v_exp_f32_e32 v125, v116
	v_mfma_f32_16x16x32_bf16 v[130:133], v[102:105], v[134:137], v[130:133]
	v_med3_f32 v121, v121, s55, v232
	v_exp_f32_e32 v124, v126
	v_exp_f32_e32 v126, v127
	v_exp_f32_e32 v127, v121
	v_mfma_f32_16x16x32_bf16 v[130:133], v[106:109], v[138:141], v[130:133]
	v_exp_f32_e32 v117, v117
	v_add_f32_e32 v115, 1.0, v115
	v_pk_add_f32 v[134:135], v[124:125], 1.0 op_sel_hi:[1,0]
	v_rcp_f32_e32 v120, v115
	v_mul_f32_e32 v115, v134, v135
	v_pk_add_f32 v[134:135], v[126:127], 1.0 op_sel_hi:[1,0]
	s_nop 1
	v_exp_f32_e32 v116, v130
	v_rcp_f32_e32 v130, v115
	v_add_f32_e32 v115, 1.0, v117
	v_mul_f32_e32 v117, v134, v135
	v_exp_f32_e32 v124, v131
	v_rcp_f32_e32 v131, v117
	v_rcp_f32_e32 v121, v115
	v_mov_b32_e32 v126, v125
	v_pk_add_f32 v[126:127], v[126:127], 1.0 op_sel_hi:[1,0] neg_lo:[1,0] neg_hi:[1,0]
	v_med3_f32 v123, v123, s55, v232
	v_pk_mul_f32 v[126:127], v[126:127], v[130:131]
	v_exp_f32_e32 v119, v119
	v_pk_fma_f32 v[168:169], v[168:169], v[120:121], v[126:127]
	s_nop 0
	v_mul_f32_e32 v115, 0xc038aa3b, v168
	v_med3_f32 v115, v115, s55, v232
	v_exp_f32_e32 v117, v115
	v_mul_f32_e32 v115, 0xc038aa3b, v169
	v_med3_f32 v115, v115, s55, v232
	v_exp_f32_e32 v125, v115
	v_pk_add_f32 v[120:121], v[116:117], 1.0 op_sel_hi:[1,0]
	v_pk_add_f32 v[126:127], v[124:125], 1.0 op_sel_hi:[1,0]
	v_mul_f32_e32 v115, v120, v121
	v_rcp_f32_e32 v120, v115
	v_mul_f32_e32 v115, v126, v127
	v_rcp_f32_e32 v121, v115
	v_mov_b32_e32 v124, v117
	v_exp_f32_e32 v115, v118
	v_med3_f32 v118, v122, s55, v232
	v_pk_add_f32 v[116:117], v[124:125], 1.0 op_sel_hi:[1,0] neg_lo:[1,0] neg_hi:[1,0]
	v_exp_f32_e32 v124, v128
	v_exp_f32_e32 v125, v118
	v_add_f32_e32 v115, 1.0, v115
	v_rcp_f32_e32 v122, v115
	v_exp_f32_e32 v118, v132
	v_pk_add_f32 v[126:127], v[124:125], 1.0 op_sel_hi:[1,0]
	v_exp_f32_e32 v124, v133
	v_mul_f32_e32 v115, v126, v127
	v_exp_f32_e32 v126, v129
	v_exp_f32_e32 v127, v123
	v_rcp_f32_e32 v128, v115
	v_add_f32_e32 v115, 1.0, v119
	v_rcp_f32_e32 v123, v115
	v_pk_add_f32 v[130:131], v[126:127], 1.0 op_sel_hi:[1,0]
	v_mov_b32_e32 v126, v125
	v_mul_f32_e32 v119, v130, v131
	v_rcp_f32_e32 v129, v119
	v_pk_add_f32 v[126:127], v[126:127], 1.0 op_sel_hi:[1,0] neg_lo:[1,0] neg_hi:[1,0]
	v_pk_mul_f32 v[116:117], v[116:117], v[120:121]
	v_pk_mul_f32 v[126:127], v[126:127], v[128:129]
	s_nop 0
	v_pk_fma_f32 v[170:171], v[170:171], v[122:123], v[126:127]
	v_cvt_pk_bf16_f32 v120, v116, v117
	v_mul_f32_e32 v115, 0xc038aa3b, v170
	v_med3_f32 v115, v115, s55, v232
	v_exp_f32_e32 v119, v115
	v_mul_f32_e32 v115, 0xc038aa3b, v171
	v_med3_f32 v115, v115, s55, v232
	v_exp_f32_e32 v125, v115
	v_pk_add_f32 v[122:123], v[118:119], 1.0 op_sel_hi:[1,0]
	v_pk_mul_f32 v[116:117], v[162:163], v[116:117]
	v_mul_f32_e32 v115, v122, v123
	v_pk_add_f32 v[126:127], v[124:125], 1.0 op_sel_hi:[1,0]
	v_rcp_f32_e32 v122, v115
	v_mul_f32_e32 v115, v126, v127
	v_rcp_f32_e32 v123, v115
	v_mov_b32_e32 v124, v119
	v_pk_add_f32 v[118:119], v[124:125], 1.0 op_sel_hi:[1,0] neg_lo:[1,0] neg_hi:[1,0]
	v_cvt_pk_bf16_f32 v116, v116, v117
	v_pk_mul_f32 v[118:119], v[118:119], v[122:123]
	v_add_u32_e32 v122, 0x100, v166
	v_cvt_pk_bf16_f32 v121, v118, v119
	v_mov_b32_e32 v123, v114
	v_pk_mul_f32 v[118:119], v[164:165], v[118:119]
	v_lshl_add_u64 v[122:123], v[122:123], 1, s[30:31]
	v_cvt_pk_bf16_f32 v117, v118, v119
	global_store_dwordx2 v[122:123], v[120:121], off nt
	ds_write_b64 v205, v[116:117] offset:4608
	s_waitcnt lgkmcnt(0)
	s_barrier
	ds_read_b128 v[134:137], v206 offset:4608
	ds_read_b128 v[138:141], v206 offset:4672
	ds_read_b128 v[142:145], v206 offset:4736
	ds_read_b128 v[146:149], v206 offset:4800
	s_and_saveexec_b64 s[42:43], s[6:7]
	s_xor_b64 s[42:43], exec, s[42:43]
	s_cbranch_execz .LBB1_165
	s_and_saveexec_b64 s[44:45], s[8:9]
	s_xor_b64 s[44:45], exec, s[44:45]
	s_cbranch_execz .LBB1_160
	s_andn2_b64 vcc, exec, s[24:25]
	s_cbranch_vccnz .LBB1_160
	s_andn2_b32 s49, 1, s59
	s_mulk_i32 s49, 0xd00
	v_lshl_add_u32 v115, s49, 2, v185
	v_add_u32_e32 v116, 0xec00, v115
	s_waitcnt vmcnt(3)
	ds_write2st64_b32 v115, v188, v187 offset0:236 offset1:249
	s_waitcnt vmcnt(1)
	ds_write2st64_b32 v116, v186, v157 offset0:26 offset1:39
	s_and_saveexec_b64 s[46:47], s[26:27]
	s_cbranch_execz .LBB1_194
	v_lshl_add_u32 v115, s49, 2, v225
	v_add_u32_e32 v116, 0xec00, v115
	ds_write2st64_b32 v115, v155, v182 offset0:236 offset1:249
	ds_write2st64_b32 v116, v183, v184 offset0:26 offset1:39
	s_or_b64 exec, exec, s[46:47]
	s_and_saveexec_b64 s[46:47], s[20:21]
	s_cbranch_execnz .LBB1_195

.LBB1_189:
	s_or_b64 exec, exec, s[44:45]
	v_sub_f32_e32 v115, v150, v176
	v_sub_f32_e32 v134, v150, v142
	v_add_f32_e64 v115, |v115|, |v134|
	v_sub_f32_e32 v134, v150, v144
	v_sub_f32_e32 v135, v151, v177
	v_sub_f32_e32 v136, v151, v143
	v_add_f32_e64 v115, v115, |v134|
	v_add_f32_e64 v135, |v135|, |v136|
	v_sub_f32_e32 v136, v151, v145
	v_fma_f32 v115, v174, v115, 0
	v_add_f32_e64 v135, v135, |v136|
	v_fmac_f32_e32 v115, v175, v135
	v_sub_f32_e32 v116, v152, v116
	v_sub_f32_e32 v135, v152, v138
	v_add_f32_e32 v134, 0, v174
	v_add_f32_e64 v116, |v116|, |v135|
	v_sub_f32_e32 v135, v152, v140
	v_add_f32_e32 v134, v175, v134
	v_add_f32_e64 v116, v116, |v135|
	v_fmac_f32_e32 v115, v172, v116
	v_add_f32_e32 v116, v172, v134
	v_sub_f32_e32 v117, v153, v117
	v_sub_f32_e32 v134, v153, v139
	v_add_f32_e64 v117, |v117|, |v134|
	v_sub_f32_e32 v134, v153, v141
	v_add_f32_e64 v117, v117, |v134|
	v_fmac_f32_e32 v115, v173, v117
	v_add_f32_e32 v116, v173, v116
	s_nop 0
	v_mov_b32_e32 v246, v115
	v_mov_b32_e32 v247, v116
.LBB1_192:
	s_or_b64 exec, exec, s[42:43]
	v_mad_u32_u24 v115, v167, s53, v226
	s_waitcnt lgkmcnt(0)
	s_barrier
	ds_read_b128 v[134:137], v115
	ds_read_b128 v[138:141], v115 offset:64
	s_waitcnt lgkmcnt(1)
	v_mfma_f32_16x16x32_bf16 v[116:119], v[18:21], v[134:137], v[118:121]
	s_and_b64 vcc, exec, s[24:25]
	v_mfma_f32_16x16x32_bf16 v[120:123], v[46:49], v[134:137], v[122:125]
	v_mfma_f32_16x16x32_bf16 v[124:127], v[74:77], v[134:137], v[126:129]
	s_waitcnt lgkmcnt(0)
	v_mfma_f32_16x16x32_bf16 v[116:119], v[22:25], v[138:141], v[116:119]
	v_mfma_f32_16x16x32_bf16 v[124:127], v[78:81], v[138:141], v[124:127]
	v_mfma_f32_16x16x32_bf16 v[120:123], v[50:53], v[138:141], v[120:123]
	s_and_b64 s[70:71], exec, s[6:7]
	s_cbranch_scc1 .Lred_skip_3
	v_add_f32_dpp v246, v246, v246 quad_perm:[1,0,3,2] row_mask:0xf bank_mask:0xf bound_ctrl:1
	v_add_f32_dpp v247, v247, v247 quad_perm:[1,0,3,2] row_mask:0xf bank_mask:0xf bound_ctrl:1
	s_nop 0
	v_add_f32_dpp v246, v246, v246 quad_perm:[2,3,0,1] row_mask:0xf bank_mask:0xf bound_ctrl:1
	v_add_f32_dpp v247, v247, v247 quad_perm:[2,3,0,1] row_mask:0xf bank_mask:0xf bound_ctrl:1
	s_nop 0
	v_add_f32_dpp v246, v246, v246 row_half_mirror row_mask:0xf bank_mask:0xf bound_ctrl:1
	v_add_f32_dpp v247, v247, v247 row_half_mirror row_mask:0xf bank_mask:0xf bound_ctrl:1
	s_nop 0
	v_add_f32_dpp v246, v246, v246 row_mirror row_mask:0xf bank_mask:0xf bound_ctrl:1
	v_add_f32_dpp v247, v247, v247 row_mirror row_mask:0xf bank_mask:0xf bound_ctrl:1
	s_nop 0
	v_readlane_b32 s62, v246, 0
	v_readlane_b32 s63, v247, 0
	v_readlane_b32 s64, v246, 16
	v_readlane_b32 s65, v247, 16
	v_readlane_b32 s66, v246, 32
	v_readlane_b32 s67, v247, 32
	v_readlane_b32 s68, v246, 48
	v_readlane_b32 s69, v247, 48
	v_mov_b32_e32 v246, s64
	v_mov_b32_e32 v247, s65
	s_nop 0
	v_pk_add_f32 v[246:247], s[62:63], v[246:247]
	s_nop 0
	v_pk_add_f32 v[246:247], v[246:247], s[66:67]
	s_nop 0
	v_pk_add_f32 v[246:247], v[246:247], s[68:69]
	s_and_saveexec_b64 s[70:71], s[18:19]
	ds_write_b64 v231, v[246:247] offset:72
	s_or_b64 exec, exec, s[70:71]
.Lred_skip_3:
	s_nop 5
	v_exp_f32_e32 v142, v116
	v_med3_f32 v116, v124, s55, v232
	v_exp_f32_e32 v143, v116
	v_mfma_f32_16x16x32_bf16 v[128:131], v[102:105], v[134:137], v[130:133]
	v_exp_f32_e32 v124, v117
	v_exp_f32_e32 v115, v120
	v_exp_f32_e32 v117, v121
	v_med3_f32 v121, v125, s55, v232
	v_exp_f32_e32 v125, v121
	v_mfma_f32_16x16x32_bf16 v[128:131], v[106:109], v[138:141], v[128:131]
	v_add_f32_e32 v115, 1.0, v115
	v_pk_add_f32 v[132:133], v[142:143], 1.0 op_sel_hi:[1,0]
	v_rcp_f32_e32 v120, v115
	v_mul_f32_e32 v115, v132, v133
	v_pk_add_f32 v[134:135], v[124:125], 1.0 op_sel_hi:[1,0]
	s_nop 2
	v_exp_f32_e32 v116, v128
	v_rcp_f32_e32 v128, v115
	v_add_f32_e32 v115, 1.0, v117
	v_mul_f32_e32 v117, v134, v135
	v_exp_f32_e32 v132, v129
	v_rcp_f32_e32 v129, v117
	v_rcp_f32_e32 v121, v115
	v_mov_b32_e32 v124, v143
	v_pk_add_f32 v[124:125], v[124:125], 1.0 op_sel_hi:[1,0] neg_lo:[1,0] neg_hi:[1,0]
	s_nop 0
	v_pk_mul_f32 v[124:125], v[124:125], v[128:129]
	s_nop 0
	v_pk_fma_f32 v[168:169], v[168:169], v[120:121], v[124:125]
	s_nop 0
	v_mul_f32_e32 v115, 0xc038aa3b, v168
	v_med3_f32 v115, v115, s55, v232
	v_exp_f32_e32 v117, v115
	v_mul_f32_e32 v115, 0xc038aa3b, v169
	v_med3_f32 v115, v115, s55, v232
	v_exp_f32_e32 v133, v115
	v_pk_add_f32 v[120:121], v[116:117], 1.0 op_sel_hi:[1,0]
	v_pk_add_f32 v[124:125], v[132:133], 1.0 op_sel_hi:[1,0]
	v_mul_f32_e32 v115, v120, v121
	v_rcp_f32_e32 v120, v115
	v_mul_f32_e32 v115, v124, v125
	v_exp_f32_e32 v124, v118
	v_med3_f32 v118, v126, s55, v232
	v_rcp_f32_e32 v121, v115
	v_exp_f32_e32 v115, v122
	v_exp_f32_e32 v125, v118
	v_exp_f32_e32 v126, v119
	v_exp_f32_e32 v119, v123
	v_med3_f32 v123, v127, s55, v232
	v_exp_f32_e32 v127, v123
	v_add_f32_e32 v115, 1.0, v115
	v_pk_add_f32 v[128:129], v[124:125], 1.0 op_sel_hi:[1,0]
	v_exp_f32_e32 v118, v130
	v_rcp_f32_e32 v122, v115
	v_mul_f32_e32 v115, v128, v129
	v_exp_f32_e32 v124, v131
	v_pk_add_f32 v[130:131], v[126:127], 1.0 op_sel_hi:[1,0]
	v_rcp_f32_e32 v128, v115
	v_add_f32_e32 v115, 1.0, v119
	v_mul_f32_e32 v119, v130, v131
	v_rcp_f32_e32 v129, v119
	v_rcp_f32_e32 v123, v115
	v_mov_b32_e32 v126, v125
	v_pk_add_f32 v[126:127], v[126:127], 1.0 op_sel_hi:[1,0] neg_lo:[1,0] neg_hi:[1,0]
	v_mov_b32_e32 v132, v117
	v_pk_mul_f32 v[126:127], v[126:127], v[128:129]
	v_pk_add_f32 v[116:117], v[132:133], 1.0 op_sel_hi:[1,0] neg_lo:[1,0] neg_hi:[1,0]
	v_pk_fma_f32 v[170:171], v[170:171], v[122:123], v[126:127]
	v_pk_mul_f32 v[116:117], v[116:117], v[120:121]
	v_mul_f32_e32 v115, 0xc038aa3b, v170
	v_med3_f32 v115, v115, s55, v232
	v_exp_f32_e32 v119, v115
	v_mul_f32_e32 v115, 0xc038aa3b, v171
	v_med3_f32 v115, v115, s55, v232
	v_exp_f32_e32 v125, v115
	v_pk_add_f32 v[122:123], v[118:119], 1.0 op_sel_hi:[1,0]
	v_cvt_pk_bf16_f32 v120, v116, v117
	v_mul_f32_e32 v115, v122, v123
	v_pk_add_f32 v[126:127], v[124:125], 1.0 op_sel_hi:[1,0]
	v_rcp_f32_e32 v122, v115
	v_mul_f32_e32 v115, v126, v127
	v_rcp_f32_e32 v123, v115
	v_mov_b32_e32 v124, v119
	v_pk_add_f32 v[118:119], v[124:125], 1.0 op_sel_hi:[1,0] neg_lo:[1,0] neg_hi:[1,0]
	s_nop 0
	v_pk_mul_f32 v[118:119], v[118:119], v[122:123]
	v_add_u32_e32 v122, 0x180, v166
	v_mov_b32_e32 v123, v114
	v_cvt_pk_bf16_f32 v121, v118, v119
	v_lshl_add_u64 v[122:123], v[122:123], 1, s[30:31]
	global_store_dwordx2 v[122:123], v[120:121], off nt
	s_cbranch_vccnz .LBB1_42
	v_pk_mul_f32 v[116:117], v[162:163], v[116:117]
	v_pk_mul_f32 v[118:119], v[164:165], v[118:119]
	v_cvt_pk_bf16_f32 v116, v116, v117
	v_cvt_pk_bf16_f32 v117, v118, v119
	ds_write_b64 v205, v[116:117]
	s_branch .LBB1_42

	.amdhsa_kernel _Z10rnn_kernelPKfS0_S0_S0_S0_S0_PKtS2_PfPtS3_
		.amdhsa_group_segment_fixed_size 0
		.amdhsa_private_segment_fixed_size 0
		.amdhsa_kernarg_size 88
		.amdhsa_user_sgpr_count 2
		.amdhsa_user_sgpr_dispatch_ptr 0
		.amdhsa_user_sgpr_queue_ptr 0
		.amdhsa_user_sgpr_kernarg_segment_ptr 1
		.amdhsa_user_sgpr_dispatch_id 0
		.amdhsa_user_sgpr_kernarg_preload_length 0
		.amdhsa_user_sgpr_kernarg_preload_offset 0
		.amdhsa_user_sgpr_private_segment_size 0
		.amdhsa_uses_dynamic_stack 0
		.amdhsa_enable_private_segment 0
		.amdhsa_system_sgpr_workgroup_id_x 1
		.amdhsa_system_sgpr_workgroup_id_y 0
		.amdhsa_system_sgpr_workgroup_id_z 0
		.amdhsa_system_sgpr_workgroup_info 0
		.amdhsa_system_vgpr_workitem_id 0
		.amdhsa_next_free_vgpr 250
		.amdhsa_next_free_sgpr 72
		.amdhsa_accum_offset 252
		.amdhsa_reserve_vcc 1
		.amdhsa_float_round_mode_32 0
		.amdhsa_float_round_mode_16_64 0
		.amdhsa_float_denorm_mode_32 3
		.amdhsa_float_denorm_mode_16_64 3
		.amdhsa_dx10_clamp 1
		.amdhsa_ieee_mode 1
		.amdhsa_fp16_overflow 0
		.amdhsa_tg_split 0
		.amdhsa_exception_fp_ieee_invalid_op 0
		.amdhsa_exception_fp_denorm_src 0
		.amdhsa_exception_fp_ieee_div_zero 0
		.amdhsa_exception_fp_ieee_overflow 0
		.amdhsa_exception_fp_ieee_underflow 0
		.amdhsa_exception_fp_ieee_inexact 0
		.amdhsa_exception_int_div_zero 0
	.end_amdhsa_kernel

.LBB2_10:
	s_setprio 0
	v_add_u32_e32 v106, v73, v112
	ds_read_b128 v[74:77], v106
	v_add_u32_e32 v94, s13, v112
	v_add_u32_e32 v78, 0x1f200, v94
	ds_read_b128 v[78:81], v78
	ds_read_b128 v[82:85], v106 offset:64
	s_waitcnt vmcnt(11) lgkmcnt(0)
	v_mfma_f32_16x16x32_bf16 v[86:89], v[74:77], v[24:27], v[78:81]
	s_waitcnt vmcnt(7)
	v_mfma_f32_16x16x32_bf16 v[90:93], v[74:77], v[64:67], v[78:81]
	s_waitcnt vmcnt(3)
	v_mfma_f32_16x16x32_bf16 v[74:77], v[74:77], v[68:71], v[78:81]
	v_mfma_f32_16x16x32_bf16 v[78:81], v[82:85], v[20:23], v[86:89]
	v_mfma_f32_16x16x32_bf16 v[86:89], v[82:85], v[56:59], v[90:93]
	s_waitcnt vmcnt(2)
	v_mfma_f32_16x16x32_bf16 v[74:77], v[82:85], v[60:63], v[74:77]
	ds_read_b128 v[82:85], v106 offset:128
	s_nop 0
	ds_read_b128 v[90:93], v106 offset:192
	s_waitcnt lgkmcnt(1)
	v_mfma_f32_16x16x32_bf16 v[86:89], v[82:85], v[40:43], v[86:89]
	v_mfma_f32_16x16x32_bf16 v[78:81], v[82:85], v[16:19], v[78:81]
	s_waitcnt vmcnt(1)
	v_mfma_f32_16x16x32_bf16 v[74:77], v[82:85], v[44:47], v[74:77]
	s_waitcnt lgkmcnt(0)
	v_mfma_f32_16x16x32_bf16 v[82:85], v[90:93], v[28:31], v[86:89]
	s_nop 2
	ds_read_b128 v[86:89], v106 offset:4352
	v_mfma_f32_16x16x32_bf16 v[78:81], v[90:93], v[12:15], v[78:81]
	s_waitcnt vmcnt(0)
	v_mfma_f32_16x16x32_bf16 v[74:77], v[90:93], v[32:35], v[74:77]
	v_add_u32_e32 v90, 0x1f240, v94
	ds_read_b128 v[90:93], v90
	ds_read_b128 v[94:97], v106 offset:4416
	s_waitcnt lgkmcnt(1)
	v_mfma_f32_16x16x32_bf16 v[98:101], v[86:89], v[24:27], v[90:93]
	v_mfma_f32_16x16x32_bf16 v[102:105], v[86:89], v[64:67], v[90:93]
	v_mfma_f32_16x16x32_bf16 v[86:89], v[86:89], v[68:71], v[90:93]
	s_waitcnt lgkmcnt(0)
	v_mfma_f32_16x16x32_bf16 v[90:93], v[94:97], v[20:23], v[98:101]
	v_mfma_f32_16x16x32_bf16 v[98:101], v[94:97], v[56:59], v[102:105]
	v_mfma_f32_16x16x32_bf16 v[86:89], v[94:97], v[60:63], v[86:89]
	ds_read_b128 v[94:97], v106 offset:4480
	s_nop 1
	ds_read_b128 v[102:105], v106 offset:4544
	s_waitcnt lgkmcnt(1)
	v_mfma_f32_16x16x32_bf16 v[90:93], v[94:97], v[16:19], v[90:93]
	v_mfma_f32_16x16x32_bf16 v[98:101], v[94:97], v[40:43], v[98:101]
	v_mfma_f32_16x16x32_bf16 v[86:89], v[94:97], v[44:47], v[86:89]
	s_waitcnt lgkmcnt(0)
	v_mfma_f32_16x16x32_bf16 v[90:93], v[102:105], v[12:15], v[90:93]
	v_mfma_f32_16x16x32_bf16 v[94:97], v[102:105], v[28:31], v[98:101]
	v_mfma_f32_16x16x32_bf16 v[86:89], v[102:105], v[32:35], v[86:89]
	s_setprio 2
	s_nop 1
	v_exp_f32_e32 v99, v78
	v_exp_f32_e32 v100, v79
	v_exp_f32_e32 v101, v80
	v_exp_f32_e32 v102, v81
	v_exp_f32_e32 v90, v90
	v_exp_f32_e32 v91, v91
	v_exp_f32_e32 v92, v92
	v_exp_f32_e32 v93, v93
	v_exp_f32_e32 v103, v74
	v_exp_f32_e32 v104, v75
	v_exp_f32_e32 v105, v76
	v_exp_f32_e32 v106, v77
	v_exp_f32_e32 v88, v88
	v_exp_f32_e32 v89, v89
	v_add_u32_e32 v98, v72, v112
	v_exp_f32_e32 v82, v82
	v_exp_f32_e32 v83, v83
	v_exp_f32_e32 v84, v84
	v_exp_f32_e32 v85, v85
	v_add_u32_e32 v74, 0x17600, v98
	v_add_u32_e32 v78, 0x1a300, v98
	v_add_f32_e32 v98, 1.0, v99
	v_add_f32_e32 v99, 1.0, v100
	v_add_f32_e32 v100, 1.0, v101
	v_add_f32_e32 v101, 1.0, v102
	v_add_f32_e32 v90, 1.0, v90
	v_add_f32_e32 v91, 1.0, v91
	v_add_f32_e32 v92, 1.0, v92
	v_add_f32_e32 v93, 1.0, v93
	v_exp_f32_e32 v94, v94
	v_exp_f32_e32 v95, v95
	v_exp_f32_e32 v96, v96
	v_exp_f32_e32 v97, v97
	v_exp_f32_e32 v86, v86
	v_exp_f32_e32 v87, v87
	ds_read_b128 v[74:77], v74
	ds_read_b128 v[78:81], v78
	v_add_f32_e32 v102, 1.0, v103
	v_add_f32_e32 v103, 1.0, v104
	v_add_f32_e32 v104, 1.0, v105
	v_add_f32_e32 v105, 1.0, v106
	v_add_f32_e32 v106, 1.0, v88
	v_add_f32_e32 v107, 1.0, v89
	v_rcp_f32_e32 v88, v98
	v_rcp_f32_e32 v89, v99
	v_rcp_f32_e32 v98, v100
	v_rcp_f32_e32 v99, v101
	v_rcp_f32_e32 v90, v90
	v_rcp_f32_e32 v91, v91
	v_rcp_f32_e32 v92, v92
	v_rcp_f32_e32 v93, v93
	v_add_f32_e32 v82, 1.0, v82
	v_add_f32_e32 v83, 1.0, v83
	v_add_f32_e32 v84, 1.0, v84
	v_add_f32_e32 v85, 1.0, v85
	v_add_f32_e32 v94, 1.0, v94
	v_add_f32_e32 v95, 1.0, v95
	v_add_f32_e32 v96, 1.0, v96
	v_add_f32_e32 v97, 1.0, v97
	v_add_f32_e32 v86, 1.0, v86
	v_add_f32_e32 v87, 1.0, v87
	v_rcp_f32_e32 v100, v82
	v_rcp_f32_e32 v101, v83
	v_rcp_f32_e32 v119, v84
	v_rcp_f32_e32 v120, v85
	v_cvt_pk_bf16_f32 v82, v88, v89
	v_cvt_pk_bf16_f32 v83, v98, v99
	v_cvt_pk_bf16_f32 v84, v90, v91
	v_cvt_pk_bf16_f32 v85, v92, v93
	v_rcp_f32_e32 v94, v94
	v_rcp_f32_e32 v95, v95
	v_rcp_f32_e32 v96, v96
	v_rcp_f32_e32 v97, v97
	v_rcp_f32_e32 v102, v102
	v_rcp_f32_e32 v103, v103
	v_rcp_f32_e32 v104, v104
	v_rcp_f32_e32 v105, v105
	s_waitcnt lgkmcnt(1)
	v_mfma_f32_16x16x32_bf16 v[52:55], v[74:77], v[82:85], v[52:55]
	v_rcp_f32_e32 v90, v86
	v_rcp_f32_e32 v91, v87
	v_rcp_f32_e32 v92, v107
	s_waitcnt lgkmcnt(0)
	v_mfma_f32_16x16x32_bf16 v[0:3], v[78:81], v[82:85], v[0:3]
	v_rcp_f32_e32 v85, v106
	v_cvt_pk_bf16_f32 v86, v100, v101
	v_cvt_pk_bf16_f32 v87, v119, v120
	v_cvt_pk_bf16_f32 v88, v94, v95
	v_cvt_pk_bf16_f32 v89, v96, v97
	v_cvt_pk_bf16_f32 v82, v102, v103
	v_cvt_pk_bf16_f32 v83, v104, v105
	v_cvt_pk_bf16_f32 v84, v90, v91
	v_cvt_pk_bf16_f32 v85, v85, v92
	v_mfma_f32_16x16x32_bf16 v[48:51], v[74:77], v[86:89], v[48:51]
	s_add_i32 s12, s12, -1
	s_addk_i32 s13, 0x80
	v_add_u32_e32 v73, 0x2200, v73
	v_mfma_f32_16x16x32_bf16 v[4:7], v[78:81], v[86:89], v[4:7]
	s_cmp_eq_u32 s12, 0
	v_add_u32_e32 v72, 64, v72
	v_mfma_f32_16x16x32_bf16 v[36:39], v[74:77], v[82:85], v[36:39]
	v_mfma_f32_16x16x32_bf16 v[8:11], v[78:81], v[82:85], v[8:11]
	s_cbranch_scc0 .LBB2_10
	ds_read_b128 v[72:75], v117
	ds_read_b128 v[76:79], v117 offset:64
	s_waitcnt lgkmcnt(1)
	v_mfma_f32_16x16x32_bf16 v[80:83], v[72:75], v[24:27], 0
	v_mfma_f32_16x16x32_bf16 v[84:87], v[72:75], v[64:67], 0
	v_mfma_f32_16x16x32_bf16 v[72:75], v[72:75], v[68:71], 0
	s_waitcnt lgkmcnt(0)
	v_mfma_f32_16x16x32_bf16 v[88:91], v[76:79], v[20:23], v[80:83]
	s_nop 3
	ds_read_b128 v[80:83], v117 offset:128
	ds_read_b128 v[96:99], v117 offset:192
	v_mfma_f32_16x16x32_bf16 v[84:87], v[76:79], v[56:59], v[84:87]
	v_mfma_f32_16x16x32_bf16 v[100:103], v[76:79], v[60:63], v[72:75]
	s_nop 2
	v_add_u32_e32 v72, 0, v112
	v_add_u32_e32 v92, 0x1f780, v72
	ds_read_b128 v[72:75], v92
	s_waitcnt lgkmcnt(2)
	v_mfma_f32_16x16x32_bf16 v[84:87], v[80:83], v[40:43], v[84:87]
	s_waitcnt lgkmcnt(0)
	v_add_f32_e32 v52, v72, v52
	v_mfma_f32_16x16x32_bf16 v[104:107], v[80:83], v[16:19], v[88:91]
	v_add_f32_e32 v48, v72, v48
	v_exp_f32_e32 v52, v52
	v_exp_f32_e32 v48, v48
	v_mfma_f32_16x16x32_bf16 v[80:83], v[80:83], v[44:47], v[100:103]
	v_add_f32_e32 v36, v72, v36
	v_exp_f32_e32 v36, v36
	v_add_f32_e32 v72, v52, v48
	v_mfma_f32_16x16x32_bf16 v[84:87], v[96:99], v[28:31], v[84:87]
	ds_read_b128 v[88:91], v117 offset:4352
	ds_read_b128 v[76:79], v117 offset:4416
	ds_read_b128 v[92:95], v92 offset:64
	v_add_f32_e32 v72, v72, v36
	v_add_f32_e32 v49, v73, v49
	v_mfma_f32_16x16x32_bf16 v[100:103], v[96:99], v[12:15], v[104:107]
	s_nop 1
	v_mul_f32_e32 v48, v48, v84
	v_exp_f32_e32 v49, v49
	v_add_f32_e32 v37, v73, v37
	v_mfma_f32_16x16x32_bf16 v[80:83], v[96:99], v[32:35], v[80:83]
	v_exp_f32_e32 v37, v37
	s_nop 0
	v_fmac_f32_e32 v48, v52, v100
	v_add_f32_e32 v52, v73, v53
	v_exp_f32_e32 v52, v52
	s_waitcnt lgkmcnt(2)
	v_mfma_f32_16x16x32_bf16 v[24:27], v[88:91], v[24:27], 0
	s_nop 0
	v_fmac_f32_e32 v48, v36, v80
	v_add_f32_dpp v36, v72, v72 quad_perm:[1,0,3,2] row_mask:0xf bank_mask:0xf bound_ctrl:1
	ds_read_b128 v[104:107], v117 offset:4480
	ds_read_b128 v[120:123], v117 offset:4544
	v_add_f32_dpp v36, v36, v36 quad_perm:[2,3,0,1] row_mask:0xf bank_mask:0xf bound_ctrl:1
	v_add_f32_dpp v48, v48, v48 quad_perm:[1,0,3,2] row_mask:0xf bank_mask:0xf bound_ctrl:1
	v_mfma_f32_16x16x32_bf16 v[64:67], v[88:91], v[64:67], 0
	v_add_f32_dpp v36, v36, v36 row_half_mirror row_mask:0xf bank_mask:0xf bound_ctrl:1
	v_add_f32_dpp v48, v48, v48 quad_perm:[2,3,0,1] row_mask:0xf bank_mask:0xf bound_ctrl:1
	v_add_f32_e32 v50, v74, v50
	v_add_f32_dpp v36, v36, v36 row_mirror row_mask:0xf bank_mask:0xf bound_ctrl:1
	v_rcp_f32_e32 v36, v36
	v_add_f32_dpp v48, v48, v48 row_half_mirror row_mask:0xf bank_mask:0xf bound_ctrl:1
	s_waitcnt lgkmcnt(3)
	v_mfma_f32_16x16x32_bf16 v[20:23], v[76:79], v[20:23], v[24:27]
	v_exp_f32_e32 v50, v50
	v_add_f32_dpp v48, v48, v48 row_mirror row_mask:0xf bank_mask:0xf bound_ctrl:1
	v_fma_f32 v36, v36, v48, 0
	v_add_f32_e32 v48, v52, v49
	v_mul_f32_e32 v49, v49, v85
	v_add_f32_e32 v48, v48, v37
	v_fmac_f32_e32 v49, v52, v101
	v_fmac_f32_e32 v49, v37, v81
	v_mfma_f32_16x16x32_bf16 v[68:71], v[88:91], v[68:71], 0
	v_add_f32_dpp v37, v48, v48 quad_perm:[1,0,3,2] row_mask:0xf bank_mask:0xf bound_ctrl:1
	v_add_f32_dpp v24, v49, v49 quad_perm:[1,0,3,2] row_mask:0xf bank_mask:0xf bound_ctrl:1
	v_add_f32_e32 v49, v74, v54
	v_add_f32_dpp v37, v37, v37 quad_perm:[2,3,0,1] row_mask:0xf bank_mask:0xf bound_ctrl:1
	v_add_f32_dpp v48, v24, v24 quad_perm:[2,3,0,1] row_mask:0xf bank_mask:0xf bound_ctrl:1
	v_mfma_f32_16x16x32_bf16 v[24:27], v[76:79], v[56:59], v[64:67]
	v_add_f32_dpp v37, v37, v37 row_half_mirror row_mask:0xf bank_mask:0xf bound_ctrl:1
	v_exp_f32_e32 v49, v49
	v_add_f32_dpp v48, v48, v48 row_half_mirror row_mask:0xf bank_mask:0xf bound_ctrl:1
	v_add_f32_dpp v37, v37, v37 row_mirror row_mask:0xf bank_mask:0xf bound_ctrl:1
	s_waitcnt lgkmcnt(1)
	v_mfma_f32_16x16x32_bf16 v[16:19], v[104:107], v[16:19], v[20:23]
	v_rcp_f32_e32 v37, v37
	v_add_f32_dpp v48, v48, v48 row_mirror row_mask:0xf bank_mask:0xf bound_ctrl:1
	v_add_f32_e32 v0, v92, v0
	v_add_f32_e32 v20, v74, v38
	v_mfma_f32_16x16x32_bf16 v[56:59], v[76:79], v[60:63], v[68:71]
	v_exp_f32_e32 v38, v20
	v_fmac_f32_e32 v36, v37, v48
	v_add_f32_e32 v4, v92, v4
	v_mfma_f32_16x16x32_bf16 v[20:23], v[104:107], v[40:43], v[24:27]
	v_mul_f32_e32 v40, v50, v86
	v_fmac_f32_e32 v40, v49, v102
	v_fmac_f32_e32 v40, v38, v82
	v_add_f32_e32 v24, v49, v50
	v_add_f32_e32 v37, v24, v38
	v_mfma_f32_16x16x32_bf16 v[24:27], v[104:107], v[44:47], v[56:59]
	v_exp_f32_e32 v0, v0
	v_exp_f32_e32 v4, v4
	v_add_f32_e32 v8, v92, v8
	s_waitcnt lgkmcnt(0)
	v_mfma_f32_16x16x32_bf16 v[12:15], v[120:123], v[12:15], v[16:19]
	v_exp_f32_e32 v8, v8
	v_add_f32_e32 v1, v93, v1
	v_add_f32_e32 v5, v93, v5
	v_add_f32_dpp v16, v37, v37 quad_perm:[1,0,3,2] row_mask:0xf bank_mask:0xf bound_ctrl:1
	v_exp_f32_e32 v1, v1
	v_exp_f32_e32 v5, v5
	v_add_f32_dpp v16, v16, v16 quad_perm:[2,3,0,1] row_mask:0xf bank_mask:0xf bound_ctrl:1
	v_add_f32_e32 v2, v94, v2
	v_exp_f32_e32 v2, v2
	v_add_f32_dpp v37, v16, v16 row_half_mirror row_mask:0xf bank_mask:0xf bound_ctrl:1
	v_mfma_f32_16x16x32_bf16 v[16:19], v[120:123], v[28:31], v[20:23]
	s_nop 0
	v_add_f32_dpp v28, v37, v37 row_mirror row_mask:0xf bank_mask:0xf bound_ctrl:1
	s_nop 0
	v_add_f32_dpp v20, v40, v40 quad_perm:[1,0,3,2] row_mask:0xf bank_mask:0xf bound_ctrl:1
	s_nop 1
	v_add_f32_dpp v29, v20, v20 quad_perm:[2,3,0,1] row_mask:0xf bank_mask:0xf bound_ctrl:1
	v_mfma_f32_16x16x32_bf16 v[20:23], v[120:123], v[32:35], v[24:27]
	s_nop 2
	v_add_f32_e32 v26, v75, v55
	v_add_f32_e32 v27, v75, v51
	v_rcp_f32_e32 v25, v28
	v_exp_f32_e32 v26, v26
	v_exp_f32_e32 v27, v27
	v_add_f32_e32 v28, v75, v39
	v_exp_f32_e32 v28, v28
	v_add_f32_dpp v24, v29, v29 row_half_mirror row_mask:0xf bank_mask:0xf bound_ctrl:1
	s_nop 1
	v_add_f32_dpp v24, v24, v24 row_mirror row_mask:0xf bank_mask:0xf bound_ctrl:1
	v_fmac_f32_e32 v36, v25, v24
	v_add_f32_e32 v24, v26, v27
	v_add_f32_e32 v24, v24, v28
	v_mul_f32_e32 v25, v27, v87
	v_fmac_f32_e32 v25, v26, v103
	v_add_f32_dpp v24, v24, v24 quad_perm:[1,0,3,2] row_mask:0xf bank_mask:0xf bound_ctrl:1
	v_fmac_f32_e32 v25, v28, v83
	s_nop 0
	v_add_f32_dpp v24, v24, v24 quad_perm:[2,3,0,1] row_mask:0xf bank_mask:0xf bound_ctrl:1
	v_add_f32_dpp v25, v25, v25 quad_perm:[1,0,3,2] row_mask:0xf bank_mask:0xf bound_ctrl:1
	s_nop 0
	v_add_f32_dpp v24, v24, v24 row_half_mirror row_mask:0xf bank_mask:0xf bound_ctrl:1
	v_add_f32_dpp v25, v25, v25 quad_perm:[2,3,0,1] row_mask:0xf bank_mask:0xf bound_ctrl:1
	s_nop 0
	v_add_f32_dpp v24, v24, v24 row_mirror row_mask:0xf bank_mask:0xf bound_ctrl:1
	v_rcp_f32_e32 v24, v24
	v_add_f32_dpp v25, v25, v25 row_half_mirror row_mask:0xf bank_mask:0xf bound_ctrl:1
	s_nop 1
	v_add_f32_dpp v25, v25, v25 row_mirror row_mask:0xf bank_mask:0xf bound_ctrl:1
	v_fmac_f32_e32 v36, v24, v25
	v_add_f32_e32 v24, v0, v4
	v_add_f32_e32 v24, v24, v8
	v_mul_f32_e32 v4, v4, v16
	v_fmac_f32_e32 v4, v0, v12
	v_add_f32_dpp v0, v24, v24 quad_perm:[1,0,3,2] row_mask:0xf bank_mask:0xf bound_ctrl:1
	v_fmac_f32_e32 v4, v8, v20
	v_add_f32_e32 v8, v93, v9
	v_add_f32_dpp v0, v0, v0 quad_perm:[2,3,0,1] row_mask:0xf bank_mask:0xf bound_ctrl:1
	v_add_f32_dpp v4, v4, v4 quad_perm:[1,0,3,2] row_mask:0xf bank_mask:0xf bound_ctrl:1
	v_exp_f32_e32 v8, v8
	v_add_f32_dpp v0, v0, v0 row_half_mirror row_mask:0xf bank_mask:0xf bound_ctrl:1
	v_add_f32_dpp v4, v4, v4 quad_perm:[2,3,0,1] row_mask:0xf bank_mask:0xf bound_ctrl:1
	s_nop 0
	v_add_f32_dpp v0, v0, v0 row_mirror row_mask:0xf bank_mask:0xf bound_ctrl:1
	v_rcp_f32_e32 v0, v0
	v_add_f32_dpp v4, v4, v4 row_half_mirror row_mask:0xf bank_mask:0xf bound_ctrl:1
	s_nop 1
	v_add_f32_dpp v4, v4, v4 row_mirror row_mask:0xf bank_mask:0xf bound_ctrl:1
	v_fmac_f32_e32 v36, v0, v4
	v_add_f32_e32 v0, v1, v5
	v_add_f32_e32 v0, v0, v8
	v_mul_f32_e32 v4, v5, v17
	v_fmac_f32_e32 v4, v1, v13
	v_add_f32_dpp v0, v0, v0 quad_perm:[1,0,3,2] row_mask:0xf bank_mask:0xf bound_ctrl:1
	v_fmac_f32_e32 v4, v8, v21
	v_add_f32_e32 v5, v94, v10
	v_add_f32_dpp v0, v0, v0 quad_perm:[2,3,0,1] row_mask:0xf bank_mask:0xf bound_ctrl:1
	v_add_f32_dpp v1, v4, v4 quad_perm:[1,0,3,2] row_mask:0xf bank_mask:0xf bound_ctrl:1
	v_add_f32_e32 v4, v94, v6
	v_add_f32_dpp v0, v0, v0 row_half_mirror row_mask:0xf bank_mask:0xf bound_ctrl:1
	v_exp_f32_e32 v4, v4
	v_add_f32_dpp v1, v1, v1 quad_perm:[2,3,0,1] row_mask:0xf bank_mask:0xf bound_ctrl:1
	v_add_f32_dpp v0, v0, v0 row_mirror row_mask:0xf bank_mask:0xf bound_ctrl:1
	v_rcp_f32_e32 v0, v0
	v_exp_f32_e32 v5, v5
	v_add_f32_dpp v1, v1, v1 row_half_mirror row_mask:0xf bank_mask:0xf bound_ctrl:1
	s_nop 1
	v_add_f32_dpp v1, v1, v1 row_mirror row_mask:0xf bank_mask:0xf bound_ctrl:1
	v_fmac_f32_e32 v36, v0, v1
	v_add_f32_e32 v0, v2, v4
	v_add_f32_e32 v0, v0, v5
	v_mul_f32_e32 v1, v4, v18
	v_fmac_f32_e32 v1, v2, v14
	v_add_f32_dpp v0, v0, v0 quad_perm:[1,0,3,2] row_mask:0xf bank_mask:0xf bound_ctrl:1
	v_fmac_f32_e32 v1, v5, v22
	v_add_f32_e32 v2, v95, v3
	v_add_f32_dpp v0, v0, v0 quad_perm:[2,3,0,1] row_mask:0xf bank_mask:0xf bound_ctrl:1
	v_add_f32_e32 v3, v95, v7
	v_add_f32_dpp v1, v1, v1 quad_perm:[1,0,3,2] row_mask:0xf bank_mask:0xf bound_ctrl:1
	v_add_f32_dpp v0, v0, v0 row_half_mirror row_mask:0xf bank_mask:0xf bound_ctrl:1
	v_exp_f32_e32 v2, v2
	v_exp_f32_e32 v3, v3
	v_add_f32_dpp v0, v0, v0 row_mirror row_mask:0xf bank_mask:0xf bound_ctrl:1
	v_rcp_f32_e32 v0, v0
	v_add_f32_e32 v4, v95, v11
	v_add_f32_dpp v1, v1, v1 quad_perm:[2,3,0,1] row_mask:0xf bank_mask:0xf bound_ctrl:1
	v_exp_f32_e32 v4, v4
	s_nop 0
	v_add_f32_dpp v1, v1, v1 row_half_mirror row_mask:0xf bank_mask:0xf bound_ctrl:1
	s_nop 1
	v_add_f32_dpp v1, v1, v1 row_mirror row_mask:0xf bank_mask:0xf bound_ctrl:1
	v_fmac_f32_e32 v36, v0, v1
	v_add_f32_e32 v0, v2, v3
	v_add_f32_e32 v0, v0, v4
	v_mul_f32_e32 v1, v3, v19
	v_fmac_f32_e32 v1, v2, v15
	v_add_f32_dpp v0, v0, v0 quad_perm:[1,0,3,2] row_mask:0xf bank_mask:0xf bound_ctrl:1
	v_fmac_f32_e32 v1, v4, v23
	s_nop 0
	v_add_f32_dpp v0, v0, v0 quad_perm:[2,3,0,1] row_mask:0xf bank_mask:0xf bound_ctrl:1
	v_add_f32_dpp v1, v1, v1 quad_perm:[1,0,3,2] row_mask:0xf bank_mask:0xf bound_ctrl:1
	s_nop 0
	v_add_f32_dpp v0, v0, v0 row_half_mirror row_mask:0xf bank_mask:0xf bound_ctrl:1
	v_add_f32_dpp v1, v1, v1 quad_perm:[2,3,0,1] row_mask:0xf bank_mask:0xf bound_ctrl:1
	s_nop 0
	v_add_f32_dpp v0, v0, v0 row_mirror row_mask:0xf bank_mask:0xf bound_ctrl:1
	v_rcp_f32_e32 v0, v0
	v_add_f32_dpp v1, v1, v1 row_half_mirror row_mask:0xf bank_mask:0xf bound_ctrl:1
	s_nop 1
	v_add_f32_dpp v1, v1, v1 row_mirror row_mask:0xf bank_mask:0xf bound_ctrl:1
	v_fmac_f32_e32 v36, v0, v1
	s_nop 0
	v_readlane_b32 s20, v36, 0
	v_readlane_b32 s23, v36, 16
	v_readlane_b32 s21, v36, 32
	v_readlane_b32 s22, v36, 48
	s_and_saveexec_b64 s[12:13], s[0:1]
	s_cbranch_execz .LBB2_8
	v_lshlrev_b64 v[0:1], 2, v[110:111]
	v_lshl_add_u64 v[2:3], s[4:5], 0, v[0:1]
	global_load_dword v4, v[2:3], off
	v_lshl_add_u64 v[2:3], s[6:7], 0, v[0:1]
	global_load_dword v5, v[2:3], off
	v_mov_b32_e32 v2, s23
	v_add_f32_e32 v2, s20, v2
	v_add_f32_e32 v2, s21, v2
	v_add_f32_e32 v2, s22, v2
	v_add_f32_e32 v6, s14, v2
	v_max_f32_e64 v7, -v6, 0
	v_mul_f32_e32 v2, 0xbfb8aa3b, v6
	v_sub_f32_e64 v8, -v6, v7
	v_exp_f32_e32 v2, v2
	v_mul_f32_e32 v3, 0xbfb8aa3b, v7
	v_mul_f32_e32 v8, 0x3fb8aa3b, v8
	v_exp_f32_e32 v3, v3
	v_exp_f32_e32 v8, v8
	v_add_f32_e32 v2, 1.0, v2
	v_rcp_f32_e32 v9, v2
	v_add_f32_e32 v2, v3, v8
	v_cmp_gt_f32_e32 vcc, s17, v2
	s_and_b64 s[20:21], vcc, exec
	s_cselect_b32 s20, 32, 0
	v_ldexp_f32 v2, v2, s20
	v_log_f32_e32 v10, v2
	v_lshl_add_u64 v[2:3], s[8:9], 0, v[0:1]
	global_store_dword v[2:3], v9, off
	v_cndmask_b32_e32 v8, 0, v118, vcc
	v_mul_f32_e32 v2, 0x3f317217, v10
	v_fma_f32 v2, v10, s18, -v2
	v_fmac_f32_e32 v2, 0x3377d1cf, v10
	v_fmac_f32_e32 v2, 0x3f317217, v10
	v_cmp_lt_f32_e64 vcc, |v10|, s19
	v_lshl_add_u64 v[0:1], s[10:11], 0, v[0:1]
	s_waitcnt vmcnt(2)
	v_fma_f32 v3, -v6, v4, v6
	v_cndmask_b32_e32 v2, v10, v2, vcc
	v_sub_f32_e32 v2, v2, v8
	v_add_f32_e32 v3, v7, v3
	v_add_f32_e32 v2, v2, v3
	s_waitcnt vmcnt(1)
	v_mul_f32_e32 v2, v5, v2
	global_store_dword v[0:1], v2, off
	s_branch .LBB2_8

amdhsa.kernels:
  - .agpr_count:     0
    .args:
      - .actual_access:  read_only
        .address_space:  global
        .offset:         0
        .size:           8
        .value_kind:     global_buffer
      - .actual_access:  read_only
        .address_space:  global
        .offset:         8
        .size:           8
        .value_kind:     global_buffer
      - .actual_access:  read_only
        .address_space:  global
        .offset:         16
        .size:           8
        .value_kind:     global_buffer
      - .actual_access:  read_only
        .address_space:  global
        .offset:         24
        .size:           8
        .value_kind:     global_buffer
      - .actual_access:  read_only
        .address_space:  global
        .offset:         32
        .size:           8
        .value_kind:     global_buffer
      - .actual_access:  read_only
        .address_space:  global
        .offset:         40
        .size:           8
        .value_kind:     global_buffer
      - .actual_access:  read_only
        .address_space:  global
        .offset:         48
        .size:           8
        .value_kind:     global_buffer
      - .actual_access:  read_only
        .address_space:  global
        .offset:         56
        .size:           8
        .value_kind:     global_buffer
      - .actual_access:  read_only
        .address_space:  global
        .offset:         64
        .size:           8
        .value_kind:     global_buffer
      - .actual_access:  read_only
        .address_space:  global
        .offset:         72
        .size:           8
        .value_kind:     global_buffer
      - .actual_access:  read_only
        .address_space:  global
        .offset:         80
        .size:           8
        .value_kind:     global_buffer
      - .actual_access:  read_only
        .address_space:  global
        .offset:         88
        .size:           8
        .value_kind:     global_buffer
      - .actual_access:  read_only
        .address_space:  global
        .offset:         96
        .size:           8
        .value_kind:     global_buffer
      - .actual_access:  read_only
        .address_space:  global
        .offset:         104
        .size:           8
        .value_kind:     global_buffer
      - .actual_access:  read_only
        .address_space:  global
        .offset:         112
        .size:           8
        .value_kind:     global_buffer
      - .actual_access:  read_only
        .address_space:  global
        .offset:         120
        .size:           8
        .value_kind:     global_buffer
      - .actual_access:  write_only
        .address_space:  global
        .offset:         128
        .size:           8
        .value_kind:     global_buffer
      - .actual_access:  write_only
        .address_space:  global
        .offset:         136
        .size:           8
        .value_kind:     global_buffer
      - .actual_access:  write_only
        .address_space:  global
        .offset:         144
        .size:           8
        .value_kind:     global_buffer
    .group_segment_fixed_size: 0
    .kernarg_segment_align: 8
    .kernarg_segment_size: 152
    .language:       OpenCL C
    .language_version:
      - 2
      - 0
    .max_flat_workgroup_size: 256
    .name:           _Z11prep_kernelPKfS0_S0_S0_S0_S0_S0_S0_S0_S0_S0_S0_S0_S0_S0_S0_PtS1_S1_
    .private_segment_fixed_size: 0
    .sgpr_count:     30
    .sgpr_spill_count: 0
    .symbol:         _Z11prep_kernelPKfS0_S0_S0_S0_S0_S0_S0_S0_S0_S0_S0_S0_S0_S0_S0_PtS1_S1_.kd
    .uniform_work_group_size: 1
    .uses_dynamic_stack: false
    .vgpr_count:     8
    .vgpr_spill_count: 0
    .wavefront_size: 64
  - .agpr_count:     0
    .args:
      - .actual_access:  read_only
        .address_space:  global
        .offset:         0
        .size:           8
        .value_kind:     global_buffer
      - .actual_access:  read_only
        .address_space:  global
        .offset:         8
        .size:           8
        .value_kind:     global_buffer
      - .actual_access:  read_only
        .address_space:  global
        .offset:         16
        .size:           8
        .value_kind:     global_buffer
      - .actual_access:  read_only
        .address_space:  global
        .offset:         24
        .size:           8
        .value_kind:     global_buffer
      - .actual_access:  read_only
        .address_space:  global
        .offset:         32
        .size:           8
        .value_kind:     global_buffer
      - .actual_access:  read_only
        .address_space:  global
        .offset:         40
        .size:           8
        .value_kind:     global_buffer
      - .actual_access:  read_only
        .address_space:  global
        .offset:         48
        .size:           8
        .value_kind:     global_buffer
      - .actual_access:  read_only
        .address_space:  global
        .offset:         56
        .size:           8
        .value_kind:     global_buffer
      - .actual_access:  write_only
        .address_space:  global
        .offset:         64
        .size:           8
        .value_kind:     global_buffer
      - .actual_access:  write_only
        .address_space:  global
        .offset:         72
        .size:           8
        .value_kind:     global_buffer
      - .actual_access:  write_only
        .address_space:  global
        .offset:         80
        .size:           8
        .value_kind:     global_buffer
    .group_segment_fixed_size: 0
    .kernarg_segment_align: 8
    .kernarg_segment_size: 88
    .language:       OpenCL C
    .language_version:
      - 2
      - 0
    .max_flat_workgroup_size: 512
    .name:           _Z10rnn_kernelPKfS0_S0_S0_S0_S0_PKtS2_PfPtS3_
    .private_segment_fixed_size: 0
    .sgpr_count:     78
    .sgpr_spill_count: 0
    .symbol:         _Z10rnn_kernelPKfS0_S0_S0_S0_S0_PKtS2_PfPtS3_.kd
    .uniform_work_group_size: 1
    .uses_dynamic_stack: false
    .vgpr_count:     250
    .vgpr_spill_count: 0
    .wavefront_size: 64
  - .agpr_count:     0
    .args:
      - .actual_access:  read_only
        .address_space:  global
        .offset:         0
        .size:           8
        .value_kind:     global_buffer
      - .actual_access:  read_only
        .address_space:  global
        .offset:         8
        .size:           8
        .value_kind:     global_buffer
      - .actual_access:  read_only
        .address_space:  global
        .offset:         16
        .size:           8
        .value_kind:     global_buffer
      - .actual_access:  read_only
        .address_space:  global
        .offset:         24
        .size:           8
        .value_kind:     global_buffer
      - .actual_access:  read_only
        .address_space:  global
        .offset:         32
        .size:           8
        .value_kind:     global_buffer
      - .actual_access:  write_only
        .address_space:  global
        .offset:         40
        .size:           8
        .value_kind:     global_buffer
      - .actual_access:  write_only
        .address_space:  global
        .offset:         48
        .size:           8
        .value_kind:     global_buffer
    .group_segment_fixed_size: 0
    .kernarg_segment_align: 8
    .kernarg_segment_size: 56
    .language:       OpenCL C
    .language_version:
      - 2
      - 0
    .max_flat_workgroup_size: 1024
    .name:           _Z11attn_kernelPKtS0_PKfS2_S2_PfS3_
    .private_segment_fixed_size: 0
    .sgpr_count:     30
    .sgpr_spill_count: 0
    .symbol:         _Z11attn_kernelPKtS0_PKfS2_S2_PfS3_.kd
    .uniform_work_group_size: 1
    .uses_dynamic_stack: false
    .vgpr_count:     124
    .vgpr_spill_count: 0
    .wavefront_size: 64
  - .agpr_count:     0
    .args:
      - .actual_access:  read_only
        .address_space:  global
        .offset:         0
        .size:           8
        .value_kind:     global_buffer
      - .actual_access:  read_only
        .address_space:  global
        .offset:         8
        .size:           8
        .value_kind:     global_buffer
      - .actual_access:  read_only
        .address_space:  global
        .offset:         16
        .size:           8
        .value_kind:     global_buffer
      - .actual_access:  write_only
        .address_space:  global
        .offset:         24
        .size:           8
        .value_kind:     global_buffer
    .group_segment_fixed_size: 192
    .kernarg_segment_align: 8
    .kernarg_segment_size: 32
    .language:       OpenCL C
    .language_version:
      - 2
      - 0
    .max_flat_workgroup_size: 1024
    .name:           _Z11loss_kernelPKfS0_S0_Pf
    .private_segment_fixed_size: 0
    .sgpr_count:     14
    .sgpr_spill_count: 0
    .symbol:         _Z11loss_kernelPKfS0_S0_Pf.kd
    .uniform_work_group_size: 1
    .uses_dynamic_stack: false
    .vgpr_count:     46
    .vgpr_spill_count: 0
    .wavefront_size: 64
